# v40 + flat grid-barrier release: non-last workgroups spin on the top-level generation word instead of the per-XCD relay word
# speedup vs baseline: 1.0054x; 1.0054x over previous
.LBB0_241:
	s_lshl_b32 s18, s33, 6
	s_add_i32 s92, s18, 0x500
	s_lshl_b64 s[0:1], s[92:93], 2
	v_lshl_add_u64 v[8:9], v[4:5], 0, s[0:1]
	v_mov_b32_e32 v1, 1
	flat_atomic_add v1, v[8:9], v1 sc0
	v_cvt_f32_u32_e32 v7, v6
	v_sub_u32_e32 v8, 0, v6
	v_rcp_iflag_f32_e32 v7, v7
	s_nop 0
	v_mul_f32_e32 v7, 0x4f7ffffe, v7
	v_cvt_u32_f32_e32 v7, v7
	v_mul_lo_u32 v8, v8, v7
	v_mul_hi_u32 v8, v7, v8
	v_add_u32_e32 v7, v7, v8
	s_waitcnt vmcnt(0) lgkmcnt(0)
	v_mul_hi_u32 v7, v1, v7
	v_mul_lo_u32 v9, v7, v6
	v_add_u32_e32 v8, 1, v1
	v_sub_u32_e32 v1, v1, v9
	v_add_u32_e32 v10, 1, v7
	v_cmp_ge_u32_e32 vcc, v1, v6
	v_sub_u32_e32 v9, v1, v6
	s_nop 0
	v_cndmask_b32_e32 v7, v7, v10, vcc
	v_cndmask_b32_e32 v1, v1, v9, vcc
	v_add_u32_e32 v9, 1, v7
	v_cmp_ge_u32_e32 vcc, v1, v6
	s_nop 1
	v_cndmask_b32_e32 v1, v7, v9, vcc
	v_mad_u64_u32 v[6:7], s[0:1], v6, v1, v[6:7]
	v_cmp_ne_u32_e32 vcc, v8, v6
	s_and_saveexec_b64 s[0:1], vcc
	s_xor_b64 s[0:1], exec, s[0:1]
	s_cbranch_execz .LBB0_254
	s_movk_i32 s92, 0xd40
	s_lshl_b64 s[2:3], s[92:93], 2
	v_lshl_add_u64 v[6:7], v[4:5], 0, s[2:3]
	flat_load_dword v2, v[6:7] sc1
	s_waitcnt vmcnt(0) lgkmcnt(0)
	v_cmp_eq_u32_e32 vcc, v2, v1
	s_and_saveexec_b64 s[2:3], vcc
	s_cbranch_execz .LBB0_253
	s_mov_b32 s19, 1
	s_mov_b64 s[4:5], 0
	s_branch .LBB0_245

.LBB0_483:
	s_lshl_b32 s18, s34, 6
	s_add_i32 s92, s18, 0x500
	s_lshl_b64 s[0:1], s[92:93], 2
	v_lshl_add_u64 v[8:9], v[4:5], 0, s[0:1]
	v_mov_b32_e32 v1, 1
	flat_atomic_add v7, v[8:9], v1 sc0
	v_cvt_f32_u32_e32 v1, v6
	v_sub_u32_e32 v8, 0, v6
	v_rcp_iflag_f32_e32 v1, v1
	s_nop 0
	v_mul_f32_e32 v1, 0x4f7ffffe, v1
	v_cvt_u32_f32_e32 v1, v1
	v_mul_lo_u32 v8, v8, v1
	v_mul_hi_u32 v8, v1, v8
	v_add_u32_e32 v1, v1, v8
	s_waitcnt vmcnt(0) lgkmcnt(0)
	v_mul_hi_u32 v1, v7, v1
	v_mul_lo_u32 v8, v1, v6
	v_sub_u32_e32 v8, v7, v8
	v_cmp_ge_u32_e32 vcc, v8, v6
	v_add_u32_e32 v9, 1, v1
	s_nop 0
	v_cndmask_b32_e32 v1, v1, v9, vcc
	v_sub_u32_e32 v9, v8, v6
	v_cndmask_b32_e32 v8, v8, v9, vcc
	v_cmp_ge_u32_e32 vcc, v8, v6
	v_add_u32_e32 v8, 1, v1
	s_nop 0
	v_cndmask_b32_e32 v1, v1, v8, vcc
	v_add_u32_e32 v8, 1, v7
	v_mad_u64_u32 v[6:7], s[0:1], v6, v1, v[6:7]
	v_cmp_ne_u32_e32 vcc, v8, v6
	s_and_saveexec_b64 s[0:1], vcc
	s_xor_b64 s[0:1], exec, s[0:1]
	s_cbranch_execz .LBB0_496
	s_movk_i32 s92, 0xd40
	s_lshl_b64 s[2:3], s[92:93], 2
	v_lshl_add_u64 v[6:7], v[4:5], 0, s[2:3]
	flat_load_dword v2, v[6:7] sc1
	s_waitcnt vmcnt(0) lgkmcnt(0)
	v_cmp_eq_u32_e32 vcc, v2, v1
	s_and_saveexec_b64 s[2:3], vcc
	s_cbranch_execz .LBB0_495
	s_mov_b32 s19, 1
	s_mov_b64 s[4:5], 0
	s_branch .LBB0_487

.LBB0_1095:
	s_lshl_b32 s20, s33, 6
	s_add_i32 s92, s20, 0x500
	s_lshl_b64 s[0:1], s[92:93], 2
	v_lshl_add_u64 v[8:9], v[4:5], 0, s[0:1]
	v_mov_b32_e32 v1, 1
	flat_atomic_add v7, v[8:9], v1 sc0
	v_cvt_f32_u32_e32 v1, v6
	v_sub_u32_e32 v8, 0, v6
	v_rcp_iflag_f32_e32 v1, v1
	s_nop 0
	v_mul_f32_e32 v1, 0x4f7ffffe, v1
	v_cvt_u32_f32_e32 v1, v1
	v_mul_lo_u32 v8, v8, v1
	v_mul_hi_u32 v8, v1, v8
	v_add_u32_e32 v1, v1, v8
	s_waitcnt vmcnt(0) lgkmcnt(0)
	v_mul_hi_u32 v1, v7, v1
	v_mul_lo_u32 v8, v1, v6
	v_sub_u32_e32 v8, v7, v8
	v_cmp_ge_u32_e32 vcc, v8, v6
	v_add_u32_e32 v9, 1, v1
	s_nop 0
	v_cndmask_b32_e32 v1, v1, v9, vcc
	v_sub_u32_e32 v9, v8, v6
	v_cndmask_b32_e32 v8, v8, v9, vcc
	v_cmp_ge_u32_e32 vcc, v8, v6
	v_add_u32_e32 v8, 1, v1
	s_nop 0
	v_cndmask_b32_e32 v1, v1, v8, vcc
	v_add_u32_e32 v8, 1, v7
	v_mad_u64_u32 v[6:7], s[0:1], v6, v1, v[6:7]
	v_cmp_ne_u32_e32 vcc, v8, v6
	s_and_saveexec_b64 s[0:1], vcc
	s_xor_b64 s[0:1], exec, s[0:1]
	s_cbranch_execz .LBB0_1108
	s_movk_i32 s92, 0xd40
	s_lshl_b64 s[4:5], s[92:93], 2
	v_lshl_add_u64 v[6:7], v[4:5], 0, s[4:5]
	flat_load_dword v2, v[6:7] sc1
	s_waitcnt vmcnt(0) lgkmcnt(0)
	v_cmp_eq_u32_e32 vcc, v2, v1
	s_and_saveexec_b64 s[4:5], vcc
	s_cbranch_execz .LBB0_1107
	s_mov_b32 s21, 1
	s_mov_b64 s[6:7], 0
	s_branch .LBB0_1099

.LBB0_1358:
	s_lshl_b32 s18, s33, 6
	s_add_i32 s92, s18, 0x500
	s_lshl_b64 s[0:1], s[92:93], 2
	v_lshl_add_u64 v[8:9], v[4:5], 0, s[0:1]
	v_mov_b32_e32 v1, 1
	flat_atomic_add v7, v[8:9], v1 sc0
	v_cvt_f32_u32_e32 v1, v6
	v_sub_u32_e32 v8, 0, v6
	v_rcp_iflag_f32_e32 v1, v1
	s_nop 0
	v_mul_f32_e32 v1, 0x4f7ffffe, v1
	v_cvt_u32_f32_e32 v1, v1
	v_mul_lo_u32 v8, v8, v1
	v_mul_hi_u32 v8, v1, v8
	v_add_u32_e32 v1, v1, v8
	s_waitcnt vmcnt(0) lgkmcnt(0)
	v_mul_hi_u32 v1, v7, v1
	v_mul_lo_u32 v8, v1, v6
	v_sub_u32_e32 v8, v7, v8
	v_cmp_ge_u32_e32 vcc, v8, v6
	v_add_u32_e32 v9, 1, v1
	s_nop 0
	v_cndmask_b32_e32 v1, v1, v9, vcc
	v_sub_u32_e32 v9, v8, v6
	v_cndmask_b32_e32 v8, v8, v9, vcc
	v_cmp_ge_u32_e32 vcc, v8, v6
	v_add_u32_e32 v8, 1, v1
	s_nop 0
	v_cndmask_b32_e32 v1, v1, v8, vcc
	v_add_u32_e32 v8, 1, v7
	v_mad_u64_u32 v[6:7], s[0:1], v6, v1, v[6:7]
	v_cmp_ne_u32_e32 vcc, v8, v6
	s_and_saveexec_b64 s[0:1], vcc
	s_xor_b64 s[0:1], exec, s[0:1]
	s_cbranch_execz .LBB0_1371
	s_movk_i32 s92, 0xd40
	s_lshl_b64 s[2:3], s[92:93], 2
	v_lshl_add_u64 v[6:7], v[4:5], 0, s[2:3]
	flat_load_dword v2, v[6:7] sc1
	s_waitcnt vmcnt(0) lgkmcnt(0)
	v_cmp_eq_u32_e32 vcc, v2, v1
	s_and_saveexec_b64 s[2:3], vcc
	s_cbranch_execz .LBB0_1370
	s_mov_b32 s19, 1
	s_mov_b64 s[4:5], 0
	s_branch .LBB0_1362

.LBB0_1738:
	s_lshl_b32 s18, s33, 6
	s_add_i32 s92, s18, 0x500
	s_lshl_b64 s[0:1], s[92:93], 2
	v_lshl_add_u64 v[8:9], v[4:5], 0, s[0:1]
	v_mov_b32_e32 v1, 1
	flat_atomic_add v7, v[8:9], v1 sc0
	v_cvt_f32_u32_e32 v1, v6
	v_sub_u32_e32 v8, 0, v6
	v_rcp_iflag_f32_e32 v1, v1
	s_nop 0
	v_mul_f32_e32 v1, 0x4f7ffffe, v1
	v_cvt_u32_f32_e32 v1, v1
	v_mul_lo_u32 v8, v8, v1
	v_mul_hi_u32 v8, v1, v8
	v_add_u32_e32 v1, v1, v8
	s_waitcnt vmcnt(0) lgkmcnt(0)
	v_mul_hi_u32 v1, v7, v1
	v_mul_lo_u32 v8, v1, v6
	v_sub_u32_e32 v8, v7, v8
	v_cmp_ge_u32_e32 vcc, v8, v6
	v_add_u32_e32 v9, 1, v1
	s_nop 0
	v_cndmask_b32_e32 v1, v1, v9, vcc
	v_sub_u32_e32 v9, v8, v6
	v_cndmask_b32_e32 v8, v8, v9, vcc
	v_cmp_ge_u32_e32 vcc, v8, v6
	v_add_u32_e32 v8, 1, v1
	s_nop 0
	v_cndmask_b32_e32 v1, v1, v8, vcc
	v_add_u32_e32 v8, 1, v7
	v_mad_u64_u32 v[6:7], s[0:1], v6, v1, v[6:7]
	v_cmp_ne_u32_e32 vcc, v8, v6
	s_and_saveexec_b64 s[0:1], vcc
	s_xor_b64 s[0:1], exec, s[0:1]
	v_readlane_b32 s26, v255, 25
	s_cbranch_execz .LBB0_1751
	s_movk_i32 s92, 0xd40
	s_lshl_b64 s[2:3], s[92:93], 2
	v_lshl_add_u64 v[6:7], v[4:5], 0, s[2:3]
	flat_load_dword v2, v[6:7] sc1
	s_waitcnt vmcnt(0) lgkmcnt(0)
	v_cmp_eq_u32_e32 vcc, v2, v1
	s_and_saveexec_b64 s[2:3], vcc
	s_cbranch_execz .LBB0_1750
	s_mov_b32 s19, 1
	s_mov_b64 s[4:5], 0
	s_branch .LBB0_1742
